# attention FIXM units: no static priority raise for waves 4-7 (both waves of a SIMD run the same interleaved fast path)
# speedup vs baseline: 1.0241x; 1.0005x over previous
.LBB0_1662:
	s_or_b64 exec, exec, s[14:15]
	s_lshl_b32 s14, s88, 7
	s_cmp_gt_i32 s20, 3
	s_cselect_b64 s[42:43], -1, 0
	s_cmp_lt_i32 s20, 4
	s_cbranch_scc1 .LBB0_1664
	s_setprio 0

.LBB0_1743:
	s_or_b64 exec, exec, s[14:15]
	s_lshl_b32 s14, s21, 6
	s_cmp_gt_i32 s20, 3
	s_cselect_b64 s[42:43], -1, 0
	s_cmp_lt_i32 s20, 4
	s_cbranch_scc1 .LBB0_1745
	s_setprio 0

.LBB0_1826:
	s_or_b64 exec, exec, s[14:15]
	s_cmp_gt_i32 s21, 3
	s_cselect_b64 s[52:53], -1, 0
	s_cmp_lt_i32 s21, 4
	s_cbranch_scc1 .LBB0_1828
	s_setprio 0
